# mixer heads: 14 of the 20 gate-row / spatial-weight loads hoisted above the LayerNorm section (were issued behind the barrier right before use)
# baseline (speedup 1.0000x reference)
.LBB0_366:
	s_lshl_b64 s[2:3], s[24:25], 1
	v_lshl_add_u64 v[104:105], v[170:171], 0, s[2:3]
	v_lshl_add_u64 v[106:107], v[104:105], 0, v[176:177]
	global_load_dwordx4 v[140:143], v[106:107], off
	v_lshl_add_u64 v[106:107], v[104:105], 0, v[178:179]
	global_load_dwordx4 v[136:139], v[106:107], off
	v_add_u32_e32 v116, s27, v210
	v_mov_b32_e32 v104, v116
	v_ashrrev_i32_e32 v105, 31, v104
	v_lshlrev_b64 v[104:105], 8, v[104:105]
	v_lshl_add_u64 v[104:105], v[172:173], 0, v[104:105]
	global_load_dwordx4 v[240:243], v[104:105], off
	global_load_dwordx4 v[152:155], v[104:105], off offset:64
	global_load_dwordx4 v[148:151], v[104:105], off offset:128
	global_load_dwordx4 v[144:147], v[104:105], off offset:192
	v_or_b32_e32 v104, 16, v116
	v_ashrrev_i32_e32 v105, 31, v104
	v_lshlrev_b64 v[104:105], 8, v[104:105]
	v_lshl_add_u64 v[104:105], v[172:173], 0, v[104:105]
	global_load_dwordx4 v[132:135], v[104:105], off
	global_load_dwordx4 v[128:131], v[104:105], off offset:64
	global_load_dwordx4 v[124:127], v[104:105], off offset:128
	global_load_dwordx4 v[120:123], v[104:105], off offset:192
	v_or_b32_e32 v104, 32, v116
	v_ashrrev_i32_e32 v105, 31, v104
	v_lshlrev_b64 v[104:105], 8, v[104:105]
	v_lshl_add_u64 v[104:105], v[172:173], 0, v[104:105]
	global_load_dwordx4 v[116:119], v[104:105], off
	global_load_dwordx4 v[112:115], v[104:105], off offset:64
	global_load_dwordx4 v[108:111], v[104:105], off offset:128
	global_load_dwordx4 v[104:107], v[104:105], off offset:192
	s_waitcnt vmcnt(28)
	v_lshlrev_b32_e32 v80, 16, v52
	v_and_b32_e32 v76, 0xffff0000, v52
	v_lshlrev_b32_e32 v67, 16, v48
	v_and_b32_e32 v64, 0xffff0000, v48
	s_waitcnt vmcnt(27)
	v_lshlrev_b32_e32 v81, 16, v60
	v_and_b32_e32 v78, 0xffff0000, v60
	v_lshlrev_b32_e32 v65, 16, v49
	v_and_b32_e32 v60, 0xffff0000, v49
	v_lshlrev_b32_e32 v52, 16, v51
	v_and_b32_e32 v48, 0xffff0000, v51
	s_waitcnt vmcnt(26)
	v_lshlrev_b32_e32 v51, 16, v59
	v_and_b32_e32 v49, 0xffff0000, v59
	v_add_f32_e32 v59, 0, v80
	v_lshlrev_b32_e32 v77, 16, v53
	v_add_f32_e32 v59, v59, v76
	v_and_b32_e32 v74, 0xffff0000, v53
	v_add_f32_e32 v59, v59, v77
	v_lshlrev_b32_e32 v72, 16, v54
	v_add_f32_e32 v59, v59, v74
	v_and_b32_e32 v69, 0xffff0000, v54
	v_add_f32_e32 v59, v59, v72
	v_lshlrev_b32_e32 v73, 16, v62
	v_and_b32_e32 v70, 0xffff0000, v62
	v_lshlrev_b32_e32 v62, 16, v55
	v_add_f32_e32 v59, v59, v69
	v_and_b32_e32 v55, 0xffff0000, v55
	v_add_f32_e32 v59, v59, v62
	v_add_f32_e32 v59, v59, v55
	v_add_f32_e32 v59, v59, v67
	v_add_f32_e32 v59, v59, v64
	v_add_f32_e32 v59, v59, v65
	v_lshlrev_b32_e32 v54, 16, v50
	v_add_f32_e32 v59, v59, v60
	v_and_b32_e32 v83, 64, v201
	v_and_b32_e32 v50, 0xffff0000, v50
	v_add_f32_e32 v59, v59, v54
	v_xor_b32_e32 v82, 1, v201
	v_add_u32_e32 v156, 64, v83
	v_add_f32_e32 v59, v59, v50
	v_cmp_lt_i32_e32 vcc, v82, v156
	v_add_f32_e32 v59, v59, v52
	v_add_f32_e32 v59, v59, v48
	v_cndmask_b32_e32 v82, v201, v82, vcc
	v_lshlrev_b32_e32 v82, 2, v82
	ds_bpermute_b32 v83, v82, v59
	v_lshlrev_b32_e32 v68, 16, v56
	v_and_b32_e32 v66, 0xffff0000, v56
	v_lshlrev_b32_e32 v56, 16, v58
	v_and_b32_e32 v53, 0xffff0000, v58
	s_waitcnt lgkmcnt(0)
	v_add_f32_e32 v59, v59, v83
	v_xor_b32_e32 v83, 2, v201
	v_cmp_lt_i32_e32 vcc, v83, v156
	v_lshlrev_b32_e32 v71, 16, v63
	v_and_b32_e32 v58, 0xffff0000, v63
	v_add_f32_e32 v63, 0, v81
	v_cndmask_b32_e32 v83, v201, v83, vcc
	v_lshlrev_b32_e32 v79, 16, v61
	v_add_f32_e32 v63, v63, v78
	v_lshlrev_b32_e32 v83, 2, v83
	v_and_b32_e32 v75, 0xffff0000, v61
	v_add_f32_e32 v63, v63, v79
	ds_bpermute_b32 v84, v83, v59
	v_add_f32_e32 v63, v63, v75
	v_add_f32_e32 v63, v63, v73
	v_add_f32_e32 v63, v63, v70
	v_add_f32_e32 v63, v63, v71
	v_add_f32_e32 v63, v63, v58
	s_waitcnt lgkmcnt(0)
	v_add_f32_e32 v59, v59, v84
	v_xor_b32_e32 v84, 4, v201
	v_add_f32_e32 v63, v63, v68
	v_cmp_lt_i32_e32 vcc, v84, v156
	v_lshlrev_b32_e32 v61, 16, v57
	v_add_f32_e32 v63, v63, v66
	v_cndmask_b32_e32 v84, v201, v84, vcc
	v_and_b32_e32 v57, 0xffff0000, v57
	v_add_f32_e32 v63, v63, v61
	v_lshlrev_b32_e32 v84, 2, v84
	v_add_f32_e32 v63, v63, v57
	ds_bpermute_b32 v85, v84, v59
	v_add_f32_e32 v63, v63, v56
	v_add_f32_e32 v63, v63, v53
	v_add_f32_e32 v63, v63, v51
	v_add_f32_e32 v63, v63, v49
	s_waitcnt lgkmcnt(0)
	v_add_f32_e32 v59, v59, v85
	ds_bpermute_b32 v85, v82, v63
	v_fmac_f32_e32 v76, 0xbc000000, v59
	v_fmac_f32_e32 v80, 0xbc000000, v59
	v_fmac_f32_e32 v77, 0xbc000000, v59
	v_fmac_f32_e32 v74, 0xbc000000, v59
	s_waitcnt lgkmcnt(0)
	v_add_f32_e32 v63, v63, v85
	ds_bpermute_b32 v85, v83, v63
	v_fmac_f32_e32 v72, 0xbc000000, v59
	v_fmac_f32_e32 v69, 0xbc000000, v59
	v_fmac_f32_e32 v62, 0xbc000000, v59
	v_fmac_f32_e32 v55, 0xbc000000, v59
	s_waitcnt lgkmcnt(0)
	v_add_f32_e32 v63, v63, v85
	ds_bpermute_b32 v85, v84, v63
	v_fmac_f32_e32 v67, 0xbc000000, v59
	v_fmac_f32_e32 v64, 0xbc000000, v59
	v_fmac_f32_e32 v65, 0xbc000000, v59
	v_fmac_f32_e32 v60, 0xbc000000, v59
	s_waitcnt lgkmcnt(0)
	v_add_f32_e32 v63, v63, v85
	v_mul_f32_e32 v85, v76, v76
	v_fmac_f32_e32 v85, v80, v80
	v_fmac_f32_e32 v85, v77, v77
	v_fmac_f32_e32 v85, v74, v74
	v_fmac_f32_e32 v85, v72, v72
	v_fmac_f32_e32 v85, v69, v69
	v_fmac_f32_e32 v85, v62, v62
	v_fmac_f32_e32 v85, v55, v55
	v_fmac_f32_e32 v85, v67, v67
	v_fmac_f32_e32 v85, v64, v64
	v_fmac_f32_e32 v85, v65, v65
	v_fmac_f32_e32 v85, v60, v60
	v_fmac_f32_e32 v54, 0xbc000000, v59
	v_fmac_f32_e32 v85, v54, v54
	v_fmac_f32_e32 v50, 0xbc000000, v59
	v_fmac_f32_e32 v85, v50, v50
	v_fmac_f32_e32 v52, 0xbc000000, v59
	v_fmac_f32_e32 v85, v52, v52
	v_fmac_f32_e32 v48, 0xbc000000, v59
	v_fmac_f32_e32 v85, v48, v48
	v_fmac_f32_e32 v78, 0xbc000000, v63
	ds_bpermute_b32 v59, v82, v85
	v_fmac_f32_e32 v81, 0xbc000000, v63
	v_mul_f32_e32 v86, v78, v78
	v_fmac_f32_e32 v86, v81, v81
	v_fmac_f32_e32 v79, 0xbc000000, v63
	v_fmac_f32_e32 v86, v79, v79
	v_fmac_f32_e32 v75, 0xbc000000, v63
	v_fmac_f32_e32 v86, v75, v75
	v_fmac_f32_e32 v73, 0xbc000000, v63
	v_fmac_f32_e32 v86, v73, v73
	v_fmac_f32_e32 v70, 0xbc000000, v63
	s_waitcnt lgkmcnt(0)
	v_add_f32_e32 v59, v85, v59
	v_fmac_f32_e32 v86, v70, v70
	v_fmac_f32_e32 v71, 0xbc000000, v63
	v_fmac_f32_e32 v58, 0xbc000000, v63
	v_fmac_f32_e32 v68, 0xbc000000, v63
	v_fmac_f32_e32 v66, 0xbc000000, v63
	v_fmac_f32_e32 v61, 0xbc000000, v63
	v_fmac_f32_e32 v57, 0xbc000000, v63
	v_fmac_f32_e32 v56, 0xbc000000, v63
	v_fmac_f32_e32 v53, 0xbc000000, v63
	v_fmac_f32_e32 v51, 0xbc000000, v63
	v_fmac_f32_e32 v49, 0xbc000000, v63
	ds_bpermute_b32 v63, v83, v59
	v_fmac_f32_e32 v86, v71, v71
	v_fmac_f32_e32 v86, v58, v58
	v_fmac_f32_e32 v86, v68, v68
	v_fmac_f32_e32 v86, v66, v66
	v_fmac_f32_e32 v86, v61, v61
	s_waitcnt lgkmcnt(0)
	v_add_f32_e32 v59, v59, v63
	v_fmac_f32_e32 v86, v57, v57
	ds_bpermute_b32 v63, v84, v59
	v_fmac_f32_e32 v86, v56, v56
	v_fmac_f32_e32 v86, v53, v53
	v_fmac_f32_e32 v86, v51, v51
	v_fmac_f32_e32 v86, v49, v49
	s_waitcnt lgkmcnt(0)
	v_add_f32_e32 v59, v59, v63
	ds_bpermute_b32 v63, v82, v86
	v_fmamk_f32 v59, v59, 0x3c000000, v163
	v_cmp_gt_f32_e32 vcc, s19, v59
	s_and_b32 s2, s16, 0x8000
	s_add_i32 s26, s2, 0
	s_waitcnt lgkmcnt(0)
	v_add_f32_e32 v63, v86, v63
	ds_bpermute_b32 v82, v83, v63
	s_lshl_b32 s28, s27, 2
	v_add_u32_e32 v248, s28, v238
	s_waitcnt vmcnt(21)
	v_mul_f32_e32 v0, 0x43800000, v0
	s_waitcnt vmcnt(20)
	v_mul_f32_e32 v4, 0x43800000, v4
	s_waitcnt lgkmcnt(0)
	v_add_f32_e32 v63, v63, v82
	ds_bpermute_b32 v82, v84, v63
	v_mul_f32_e32 v1, 0x43800000, v1
	s_waitcnt vmcnt(19)
	v_mul_f32_e32 v20, 0x43800000, v20
	s_waitcnt vmcnt(18)
	v_mul_f32_e32 v24, 0x43800000, v24
	s_waitcnt lgkmcnt(0)
	v_add_f32_e32 v63, v63, v82
	v_mul_f32_e32 v82, 0x4f800000, v59
	v_cndmask_b32_e32 v59, v59, v82, vcc
	v_sqrt_f32_e32 v82, v59
	s_nop 0
	v_add_u32_e32 v83, -1, v82
	v_fma_f32 v84, -v83, v82, v59
	v_cmp_ge_f32_e64 s[2:3], 0, v84
	v_add_u32_e32 v84, 1, v82
	s_nop 0
	v_cndmask_b32_e64 v83, v82, v83, s[2:3]
	v_fma_f32 v82, -v84, v82, v59
	v_cmp_lt_f32_e64 s[2:3], 0, v82
	s_nop 1
	v_cndmask_b32_e64 v82, v83, v84, s[2:3]
	v_mul_f32_e32 v83, 0x37800000, v82
	v_cndmask_b32_e32 v82, v82, v83, vcc
	v_cmp_class_f32_e32 vcc, v59, v200
	s_nop 1
	v_cndmask_b32_e32 v59, v82, v59, vcc
	v_div_scale_f32 v82, s[2:3], v59, v59, 1.0
	v_rcp_f32_e32 v83, v82
	s_nop 0
	v_fma_f32 v84, -v82, v83, 1.0
	v_fmac_f32_e32 v83, v84, v83
	v_div_scale_f32 v84, vcc, 1.0, v59, 1.0
	v_mul_f32_e32 v85, v84, v83
	v_fma_f32 v86, -v82, v85, v84
	v_fmac_f32_e32 v85, v86, v83
	v_fma_f32 v82, -v82, v85, v84
	v_div_fmas_f32 v82, v82, v83, v85
	v_div_fixup_f32 v90, v82, v59, 1.0
	v_fmamk_f32 v59, v63, 0x3c000000, v163
	v_cmp_gt_f32_e32 vcc, s19, v59
	v_mul_f32_e32 v63, 0x4f800000, v59
	v_mul_f32_e32 v80, v80, v90
	v_cndmask_b32_e32 v59, v59, v63, vcc
	v_sqrt_f32_e32 v63, v59
	v_mul_f32_e32 v76, v76, v90
	v_mul_f32_e32 v74, v74, v90
	v_mul_f32_e32 v72, v72, v90
	v_add_u32_e32 v82, -1, v63
	v_fma_f32 v83, -v82, v63, v59
	v_cmp_ge_f32_e64 s[2:3], 0, v83
	v_add_u32_e32 v83, 1, v63
	v_mul_f32_e32 v69, v69, v90
	v_cndmask_b32_e64 v82, v63, v82, s[2:3]
	v_fma_f32 v63, -v83, v63, v59
	v_cmp_lt_f32_e64 s[2:3], 0, v63
	v_mul_f32_e32 v62, v62, v90
	v_mul_f32_e32 v55, v55, v90
	v_cndmask_b32_e64 v63, v82, v83, s[2:3]
	v_mul_f32_e32 v82, 0x37800000, v63
	v_cndmask_b32_e32 v63, v63, v82, vcc
	v_cmp_class_f32_e32 vcc, v59, v200
	v_mul_f32_e32 v54, v54, v90
	v_mul_f32_e32 v50, v50, v90
	v_cndmask_b32_e32 v59, v63, v59, vcc
	v_div_scale_f32 v63, s[2:3], v59, v59, 1.0
	v_rcp_f32_e32 v82, v63
	v_mul_f32_e32 v48, v48, v90
	s_lshl_b64 s[2:3], s[24:25], 1
	v_lshl_add_u64 v[198:199], v[174:175], 0, s[2:3]
	v_fma_f32 v83, -v63, v82, 1.0
	v_fmac_f32_e32 v82, v83, v82
	v_div_scale_f32 v83, vcc, 1.0, v59, 1.0
	v_mul_f32_e32 v84, v83, v82
	v_fma_f32 v85, -v63, v84, v83
	v_fmac_f32_e32 v84, v85, v82
	v_fma_f32 v63, -v63, v84, v83
	v_div_fmas_f32 v63, v63, v82, v84
	v_div_fixup_f32 v91, v63, v59, 1.0
	v_add_u32_e32 v59, s28, v169
	v_add_u32_e32 v63, s28, v209
	ds_read_b128 v[82:85], v59
	ds_read_b128 v[86:89], v63
	v_mul_f32_e32 v81, v81, v91
	v_mul_f32_e32 v78, v78, v91
	v_mul_f32_e32 v75, v75, v91
	v_mul_f32_e32 v73, v73, v91
	s_waitcnt lgkmcnt(0)
	v_fma_f32 v80, v82, v80, v86
	v_fma_f32 v81, v82, v81, v86
	v_add_u32_e32 v82, s26, v211
	v_fma_f32 v76, v83, v76, v87
	v_fma_f32 v78, v83, v78, v87
	v_cvt_pk_bf16_f32 v80, v80, v81
	v_add3_u32 v81, v82, v212, v239
	v_cvt_pk_bf16_f32 v76, v76, v78
	v_add3_u32 v78, v82, v213, v239
	ds_write_b32 v81, v80
	ds_write_b32 v78, v76 offset:256
	v_mul_f32_e32 v76, v77, v90
	v_mul_f32_e32 v77, v79, v91
	v_fma_f32 v76, v84, v76, v88
	v_fma_f32 v77, v84, v77, v88
	v_cvt_pk_bf16_f32 v76, v76, v77
	v_add3_u32 v77, v82, v214, v239
	v_fma_f32 v74, v85, v74, v89
	v_fmac_f32_e32 v89, v85, v75
	v_add3_u32 v75, v82, v215, v239
	ds_write_b32 v77, v76 offset:512
	v_cvt_pk_bf16_f32 v74, v74, v89
	ds_write_b32 v75, v74 offset:768
	ds_read_b128 v[74:77], v59 offset:16
	ds_read_b128 v[78:81], v63 offset:16
	v_mul_f32_e32 v70, v70, v91
	v_mul_f32_e32 v58, v58, v91
	v_mul_f32_e32 v57, v57, v91
	v_mul_f32_e32 v53, v53, v91
	s_waitcnt lgkmcnt(0)
	v_fma_f32 v72, v74, v72, v78
	v_fma_f32 v73, v74, v73, v78
	v_fma_f32 v69, v75, v69, v79
	v_fma_f32 v70, v75, v70, v79
	v_cvt_pk_bf16_f32 v72, v72, v73
	v_add3_u32 v73, v82, v216, v239
	v_cvt_pk_bf16_f32 v69, v69, v70
	v_add3_u32 v70, v82, v217, v239
	ds_write_b32 v73, v72 offset:1024
	ds_write_b32 v70, v69 offset:1280
	v_mul_f32_e32 v69, v71, v91
	v_fma_f32 v62, v76, v62, v80
	v_fma_f32 v69, v76, v69, v80
	v_cvt_pk_bf16_f32 v62, v62, v69
	v_add3_u32 v69, v82, v218, v239
	v_fma_f32 v55, v77, v55, v81
	v_fmac_f32_e32 v81, v77, v58
	v_add3_u32 v58, v82, v219, v239
	ds_write_b32 v69, v62 offset:1536
	v_cvt_pk_bf16_f32 v55, v55, v81
	ds_write_b32 v58, v55 offset:1792
	ds_read_b128 v[70:73], v59 offset:32
	ds_read_b128 v[74:77], v63 offset:32
	v_mul_f32_e32 v55, v67, v90
	v_mul_f32_e32 v58, v68, v91
	v_mul_f32_e32 v51, v51, v91
	v_mul_f32_e32 v49, v49, v91
	s_waitcnt lgkmcnt(0)
	v_fma_f32 v55, v55, v70, v74
	v_fma_f32 v58, v70, v58, v74
	v_cvt_pk_bf16_f32 v55, v55, v58
	v_add3_u32 v58, v82, v220, v239
	ds_write_b32 v58, v55 offset:2048
	v_mul_f32_e32 v55, v64, v90
	v_mul_f32_e32 v58, v66, v91
	v_fma_f32 v55, v55, v71, v75
	v_fma_f32 v58, v71, v58, v75
	v_cvt_pk_bf16_f32 v55, v55, v58
	v_add3_u32 v58, v82, v221, v239
	ds_write_b32 v58, v55 offset:2304
	v_mul_f32_e32 v55, v65, v90
	v_mul_f32_e32 v58, v61, v91
	v_fma_f32 v55, v55, v72, v76
	v_fma_f32 v58, v72, v58, v76
	v_cvt_pk_bf16_f32 v55, v55, v58
	v_add3_u32 v58, v82, v222, v239
	ds_write_b32 v58, v55 offset:2560
	v_mul_f32_e32 v55, v60, v90
	v_fma_f32 v55, v55, v73, v77
	v_fmac_f32_e32 v77, v73, v57
	v_add3_u32 v57, v82, v223, v239
	v_cvt_pk_bf16_f32 v55, v55, v77
	ds_write_b32 v57, v55 offset:2816
	ds_read_b128 v[58:61], v59 offset:48
	ds_read_b128 v[62:65], v63 offset:48
	v_mul_f32_e32 v55, v56, v91
	v_add_u32_e32 v72, s26, v228
	v_add_u32_e32 v80, s26, v233
	v_add_u32_e32 v73, v72, v229
	s_waitcnt lgkmcnt(0)
	v_fma_f32 v54, v54, v58, v62
	v_fma_f32 v55, v55, v58, v62
	v_fma_f32 v50, v50, v59, v63
	v_fma_f32 v53, v53, v59, v63
	v_cvt_pk_bf16_f32 v54, v54, v55
	v_add3_u32 v55, v82, v224, v239
	v_cvt_pk_bf16_f32 v50, v50, v53
	v_add3_u32 v53, v82, v225, v239
	ds_write_b32 v55, v54 offset:3072
	ds_write_b32 v53, v50 offset:3328
	v_mul_f32_e32 v50, v52, v90
	v_fma_f32 v50, v50, v60, v64
	v_fma_f32 v51, v51, v60, v64
	v_fma_f32 v48, v48, v61, v65
	v_cvt_pk_bf16_f32 v50, v50, v51
	v_add3_u32 v51, v82, v226, v239
	v_fmac_f32_e32 v65, v49, v61
	v_cvt_pk_bf16_f32 v48, v48, v65
	v_add3_u32 v49, v82, v227, v239
	ds_write_b32 v51, v50 offset:3584
	ds_write_b32 v49, v48 offset:3840
	v_lshl_add_u64 v[48:49], v[170:171], 0, s[2:3]
	v_lshl_add_u64 v[50:51], v[48:49], 0, v[176:177]
	s_waitcnt lgkmcnt(0)
	s_waitcnt lgkmcnt(0)
	s_barrier
	v_lshl_add_u64 v[50:51], v[48:49], 0, v[180:181]
	v_lshl_add_u64 v[48:49], v[48:49], 0, v[182:183]
	global_load_dwordx4 v[68:71], v[50:51], off
	global_load_dwordx4 v[60:63], v[48:49], off
	v_add_u32_e32 v48, s27, v210
	v_or_b32_e32 v48, 48, v48
	v_ashrrev_i32_e32 v49, 31, v48
	v_lshlrev_b64 v[48:49], 8, v[48:49]
	v_lshl_add_u64 v[48:49], v[172:173], 0, v[48:49]
	global_load_dwordx4 v[64:67], v[48:49], off
	global_load_dwordx4 v[56:59], v[48:49], off offset:64
	global_load_dwordx4 v[52:55], v[48:49], off offset:128
	s_nop 0
	global_load_dwordx4 v[48:51], v[48:49], off offset:192
	v_add_u32_e32 v81, v80, v234
	ds_read_b128 v[92:95], v73
	ds_read_b128 v[100:103], v81
	v_add_u32_e32 v73, v72, v230
	v_add_u32_e32 v81, v80, v235
	ds_read_b128 v[84:87], v73
	ds_read_b128 v[96:99], v81
	v_add_u32_e32 v73, v72, v231
	v_add_u32_e32 v81, v80, v236
	ds_read_b128 v[76:79], v73
	ds_read_b128 v[88:91], v81
	s_waitcnt vmcnt(6) lgkmcnt(5)
	v_mfma_f32_16x16x32_bf16 v[244:247], v[92:95], v[240:243], 0
	v_add_u32_e32 v72, v72, v232
	v_add_u32_e32 v80, v80, v237
	ds_read_b128 v[72:75], v72
	ds_read_b128 v[80:83], v80
	s_waitcnt lgkmcnt(6)
	v_mfma_f32_16x16x32_bf16 v[240:243], v[100:103], v[240:243], 0
	v_and_b32_e32 v249, 0xffff0000, v136
	v_lshlrev_b32_e32 v252, 16, v138
	v_lshlrev_b32_e32 v250, 16, v137
	s_waitcnt vmcnt(6) lgkmcnt(5)
	v_mfma_f32_16x16x32_bf16 v[244:247], v[84:87], v[152:155], v[244:247]
	v_and_b32_e32 v253, 0xffff0000, v138
	v_and_b32_e32 v251, 0xffff0000, v137
	v_lshlrev_b32_e32 v167, 16, v139
	s_waitcnt lgkmcnt(4)
	v_mfma_f32_16x16x32_bf16 v[152:155], v[96:99], v[152:155], v[240:243]
	v_and_b32_e32 v207, 0xffff0000, v139
	s_lshr_b32 s2, s23, 8
	s_and_b32 s2, s2, 8
	s_waitcnt vmcnt(6) lgkmcnt(3)
	v_mfma_f32_16x16x32_bf16 v[240:243], v[76:79], v[148:151], v[244:247]
	s_or_b32 s24, s2, s22
	s_lshl_b64 s[2:3], s[14:15], 12
	s_or_b32 s2, s2, s24
	s_waitcnt lgkmcnt(2)
	v_mfma_f32_16x16x32_bf16 v[148:151], v[88:91], v[148:151], v[152:155]
	v_lshlrev_b32_e32 v244, 16, v143
	v_and_b32_e32 v143, 0xffff0000, v143
	v_lshlrev_b32_e32 v246, 16, v136
	s_waitcnt vmcnt(6) lgkmcnt(1)
	v_mfma_f32_16x16x32_bf16 v[152:155], v[72:75], v[144:147], v[240:243]
	s_add_u32 s6, s6, 0x80
	s_addc_u32 s7, s7, 0
	s_add_u32 s4, s4, 0x100
	s_waitcnt lgkmcnt(0)
	v_mfma_f32_16x16x32_bf16 v[146:149], v[80:83], v[144:147], v[148:151]
	ds_read2_b32 v[144:145], v248 offset1:16
	v_lshlrev_b32_e32 v240, 16, v142
	v_and_b32_e32 v142, 0xffff0000, v142
	v_lshlrev_b32_e32 v150, 16, v140
	v_and_b32_e32 v140, 0xffff0000, v140
	s_waitcnt lgkmcnt(0)
	v_add_f32_e32 v151, v152, v144
	v_add_f32_e32 v152, v153, v144
	v_lshlrev_b32_e32 v153, 16, v141
	v_add_f32_e32 v154, v154, v144
	v_and_b32_e32 v141, 0xffff0000, v141
	v_add_f32_e32 v155, v155, v144
	v_add_f32_e32 v241, v144, v146
	v_add_f32_e32 v242, v144, v147
	v_add_f32_e32 v148, v144, v148
	v_add_f32_e32 v144, v144, v149
	v_mul_f32_e32 v149, v151, v150
	v_mul_f32_e32 v151, v152, v140
	v_mul_f32_e32 v155, v155, v141
	v_mul_f32_e32 v243, v242, v142
	v_mul_f32_e32 v247, v144, v143
	s_waitcnt vmcnt(6)
	v_mfma_f32_16x16x32_bf16 v[140:143], v[92:95], v[132:135], 0
	v_mul_f32_e32 v245, v148, v244
	v_mul_f32_e32 v241, v241, v240
	v_mul_f32_e32 v153, v154, v153
	v_mfma_f32_16x16x32_bf16 v[132:135], v[100:103], v[132:135], 0
	v_lshl_add_u64 v[146:147], v[198:199], 0, v[184:185]
	v_cvt_pk_bf16_f32 v136, v149, v151
	v_cvt_pk_bf16_f32 v137, v153, v155
	s_waitcnt vmcnt(6)
	v_mfma_f32_16x16x32_bf16 v[140:143], v[84:87], v[128:131], v[140:143]
	v_cvt_pk_bf16_f32 v138, v241, v243
	v_cvt_pk_bf16_f32 v139, v245, v247
	global_store_dwordx4 v[146:147], v[136:139], off
	v_mfma_f32_16x16x32_bf16 v[128:131], v[96:99], v[128:131], v[132:135]
	s_addc_u32 s5, s5, 0
	s_add_i32 s23, s23, 0x10000
	s_addk_i32 s17, 0x800
	s_waitcnt vmcnt(7)
	v_mfma_f32_16x16x32_bf16 v[132:135], v[76:79], v[124:127], v[140:143]
	s_add_i32 s16, s16, 0x8000
	s_cmpk_eq_i32 s4, 0x800
	v_mfma_f32_16x16x32_bf16 v[124:127], v[88:91], v[124:127], v[128:131]
	s_waitcnt vmcnt(5)
	v_mfma_f32_16x16x32_bf16 v[128:131], v[72:75], v[120:123], v[132:135]
	v_mfma_f32_16x16x32_bf16 v[120:123], v[80:83], v[120:123], v[124:127]
	s_nop 6
	v_add_f32_e32 v124, v128, v145
	v_mul_f32_e32 v148, v124, v246
	v_add_f32_e32 v124, v129, v145
	v_add_f32_e32 v120, v145, v120
	v_mul_f32_e32 v150, v124, v249
	v_add_f32_e32 v124, v130, v145
	v_mul_f32_e32 v240, v120, v252
	v_add_f32_e32 v120, v145, v121
	v_mul_f32_e32 v152, v124, v250
	v_add_f32_e32 v124, v131, v145
	v_mul_f32_e32 v242, v120, v253
	v_add_f32_e32 v120, v145, v122
	v_mul_f32_e32 v154, v124, v251
	v_mul_f32_e32 v244, v120, v167
	v_add_f32_e32 v120, v145, v123
	v_pk_mul_f32 v[124:125], v[150:151], v[150:151]
	v_pk_mul_f32 v[126:127], v[154:155], v[154:155]
	v_mul_f32_e32 v246, v120, v207
	v_pk_fma_f32 v[124:125], v[148:149], v[148:149], v[124:125]
	v_pk_fma_f32 v[126:127], v[152:153], v[152:153], v[126:127]
	v_pk_mul_f32 v[120:121], v[242:243], v[242:243]
	v_pk_mul_f32 v[122:123], v[246:247], v[246:247]
	v_pk_add_f32 v[124:125], v[124:125], v[126:127]
	v_pk_fma_f32 v[120:121], v[240:241], v[240:241], v[120:121]
	v_pk_fma_f32 v[122:123], v[244:245], v[244:245], v[122:123]
	v_pk_add_f32 v[124:125], v[196:197], v[124:125]
	v_pk_add_f32 v[122:123], v[120:121], v[122:123]
	v_cvt_pk_bf16_f32 v120, v148, v150
	v_cvt_pk_bf16_f32 v121, v152, v154
	v_lshlrev_b32_e32 v127, 16, v62
	v_pk_add_f32 v[196:197], v[122:123], v[124:125]
	v_cvt_pk_bf16_f32 v122, v240, v242
	v_cvt_pk_bf16_f32 v123, v244, v246
	v_lshl_add_u64 v[124:125], v[198:199], 0, v[186:187]
	global_store_dwordx4 v[124:125], v[120:123], off
	v_and_b32_e32 v124, 0xffff0000, v60
	v_lshlrev_b32_e32 v125, 16, v61
	s_waitcnt vmcnt(6)
	v_mfma_f32_16x16x32_bf16 v[120:123], v[92:95], v[116:119], 0
	v_and_b32_e32 v128, 0xffff0000, v62
	v_and_b32_e32 v126, 0xffff0000, v61
	v_lshlrev_b32_e32 v129, 16, v63
	v_mfma_f32_16x16x32_bf16 v[116:119], v[100:103], v[116:119], 0
	v_and_b32_e32 v130, 0xffff0000, v63
	s_waitcnt vmcnt(6)
	v_mfma_f32_16x16x32_bf16 v[120:123], v[84:87], v[112:115], v[120:123]
	v_mfma_f32_16x16x32_bf16 v[112:115], v[96:99], v[112:115], v[116:119]
	s_waitcnt vmcnt(6)
	v_mfma_f32_16x16x32_bf16 v[116:119], v[76:79], v[108:111], v[120:123]
	v_mfma_f32_16x16x32_bf16 v[108:111], v[88:91], v[108:111], v[112:115]
	s_nop 3
	v_lshlrev_b32_e32 v120, 16, v71
	v_and_b32_e32 v71, 0xffff0000, v71
	v_lshlrev_b32_e32 v122, 16, v60
	s_waitcnt vmcnt(6)
	v_mfma_f32_16x16x32_bf16 v[112:115], v[72:75], v[104:107], v[116:119]
	v_mfma_f32_16x16x32_bf16 v[104:107], v[80:83], v[104:107], v[108:111]
	s_nop 1
	v_lshlrev_b32_e32 v116, 16, v70
	v_and_b32_e32 v70, 0xffff0000, v70
	ds_read2_b32 v[108:109], v248 offset0:32 offset1:48
	v_lshlrev_b32_e32 v110, 16, v68
	v_and_b32_e32 v68, 0xffff0000, v68
	s_waitcnt lgkmcnt(0)
	v_add_f32_e32 v111, v112, v108
	v_add_f32_e32 v112, v113, v108
	v_lshlrev_b32_e32 v113, 16, v69
	v_add_f32_e32 v114, v114, v108
	v_and_b32_e32 v69, 0xffff0000, v69
	v_add_f32_e32 v115, v115, v108
	v_add_f32_e32 v117, v108, v104
	v_add_f32_e32 v118, v108, v105
	v_add_f32_e32 v106, v108, v106
	v_add_f32_e32 v108, v108, v107
	v_mul_f32_e32 v107, v111, v110
	v_mul_f32_e32 v111, v112, v68
	v_mul_f32_e32 v115, v115, v69
	v_mul_f32_e32 v119, v118, v70
	v_mul_f32_e32 v123, v108, v71
	s_waitcnt vmcnt(5)
	v_mfma_f32_16x16x32_bf16 v[68:71], v[92:95], v[64:67], 0
	v_mul_f32_e32 v121, v106, v120
	v_mul_f32_e32 v117, v117, v116
	v_mul_f32_e32 v113, v114, v113
	v_mfma_f32_16x16x32_bf16 v[64:67], v[100:103], v[64:67], 0
	v_lshl_add_u64 v[104:105], v[198:199], 0, v[190:191]
	v_cvt_pk_bf16_f32 v60, v107, v111
	v_cvt_pk_bf16_f32 v61, v113, v115
	s_waitcnt vmcnt(4)
	v_mfma_f32_16x16x32_bf16 v[68:71], v[84:87], v[56:59], v[68:71]
	v_cvt_pk_bf16_f32 v62, v117, v119
	v_cvt_pk_bf16_f32 v63, v121, v123
	global_store_dwordx4 v[104:105], v[60:63], off
	v_mfma_f32_16x16x32_bf16 v[56:59], v[96:99], v[56:59], v[64:67]
	s_nop 0
	v_mov_b64_e32 v[62:63], v[18:19]
	v_mov_b64_e32 v[60:61], v[16:17]
	s_waitcnt vmcnt(4)
	v_mfma_f32_16x16x32_bf16 v[64:67], v[76:79], v[52:55], v[68:71]
	v_mfma_f32_16x16x32_bf16 v[52:55], v[88:91], v[52:55], v[56:59]
	s_waitcnt vmcnt(3)
	v_mfma_f32_16x16x32_bf16 v[56:59], v[72:75], v[48:51], v[64:67]
	v_mfma_f32_16x16x32_bf16 v[48:51], v[80:83], v[48:51], v[52:55]
	s_nop 6
	v_add_f32_e32 v52, v56, v109
	v_mul_f32_e32 v106, v52, v122
	v_add_f32_e32 v52, v57, v109
	v_add_f32_e32 v48, v109, v48
	v_mul_f32_e32 v110, v52, v124
	v_add_f32_e32 v52, v58, v109
	v_mul_f32_e32 v116, v48, v127
	v_add_f32_e32 v48, v109, v49
	v_mul_f32_e32 v112, v52, v125
	v_add_f32_e32 v52, v59, v109
	v_mul_f32_e32 v118, v48, v128
	v_add_f32_e32 v48, v109, v50
	v_mul_f32_e32 v114, v52, v126
	v_mul_f32_e32 v120, v48, v129
	v_add_f32_e32 v48, v109, v51
	v_pk_mul_f32 v[52:53], v[110:111], v[110:111]
	v_pk_mul_f32 v[54:55], v[114:115], v[114:115]
	v_mul_f32_e32 v122, v48, v130
	v_pk_fma_f32 v[52:53], v[106:107], v[106:107], v[52:53]
	v_pk_fma_f32 v[54:55], v[112:113], v[112:113], v[54:55]
	v_pk_mul_f32 v[48:49], v[118:119], v[118:119]
	v_pk_mul_f32 v[50:51], v[122:123], v[122:123]
	v_pk_add_f32 v[52:53], v[52:53], v[54:55]
	v_pk_fma_f32 v[48:49], v[116:117], v[116:117], v[48:49]
	v_pk_fma_f32 v[50:51], v[120:121], v[120:121], v[50:51]
	v_pk_add_f32 v[52:53], v[188:189], v[52:53]
	v_pk_add_f32 v[50:51], v[48:49], v[50:51]
	v_cvt_pk_bf16_f32 v48, v106, v110
	v_cvt_pk_bf16_f32 v49, v112, v114
	v_mov_b64_e32 v[58:59], v[30:31]
	v_pk_add_f32 v[188:189], v[50:51], v[52:53]
	v_cvt_pk_bf16_f32 v50, v116, v118
	v_lshl_add_u64 v[52:53], v[198:199], 0, v[192:193]
	v_cvt_pk_bf16_f32 v51, v120, v122
	global_store_dwordx4 v[52:53], v[48:51], off
	v_mov_b64_e32 v[54:55], v[10:11]
	v_mov_b64_e32 v[56:57], v[28:29]
	v_mov_b32_e32 v50, v157
	v_cvt_pk_fp8_f32 v50, v0, v4
	v_mul_f32_e32 v0, 0x43800000, v32
	v_mul_f32_e32 v4, 0x43800000, v36
	v_mov_b32_e32 v51, v157
	v_cvt_pk_fp8_f32 v51, v0, v4
	v_mul_f32_e32 v4, 0x43800000, v5
	v_mov_b32_e32 v0, v157
	v_cvt_pk_fp8_f32 v0, v1, v4
	v_cvt_pk_fp8_f32 v50, v20, v24 op_sel:[0,0,1]
	v_mul_f32_e32 v20, 0x43800000, v40
	v_mul_f32_e32 v24, 0x43800000, v44
	v_cvt_pk_fp8_f32 v51, v20, v24 op_sel:[0,0,1]
	v_mul_f32_e32 v5, 0x43800000, v21
	v_mul_f32_e32 v20, 0x43800000, v25
	v_cvt_pk_fp8_f32 v0, v5, v20 op_sel:[0,0,1]
	v_mul_f32_e32 v4, 0x43800000, v33
	v_mul_f32_e32 v5, 0x43800000, v37
	v_mov_b32_e32 v1, v157
	v_cvt_pk_fp8_f32 v1, v4, v5
	v_mov_b32_e32 v49, s3
	v_or_b32_e32 v48, s2, v162
	v_readlane_b32 s2, v254, 55
	v_mul_f32_e32 v20, 0x43800000, v41
	v_mul_f32_e32 v21, 0x43800000, v45
	v_lshlrev_b64 v[48:49], 11, v[48:49]
	v_readlane_b32 s3, v254, 56
	v_cvt_pk_fp8_f32 v1, v20, v21 op_sel:[0,0,1]
	v_mul_f32_e32 v4, 0x43800000, v22
	v_lshl_add_u64 v[48:49], s[2:3], 0, v[48:49]
	v_lshl_add_u64 v[48:49], v[48:49], 0, s[0:1]
	v_lshl_add_u64 v[48:49], v[48:49], 0, v[160:161]
	global_store_dwordx2 v[48:49], v[0:1], off offset:2048
	v_mul_f32_e32 v1, 0x43800000, v2
	v_mul_f32_e32 v2, 0x43800000, v6
	v_mov_b32_e32 v0, v157
	v_cvt_pk_fp8_f32 v0, v1, v2
	v_mul_f32_e32 v5, 0x43800000, v26
	v_mul_f32_e32 v2, 0x43800000, v34
	v_mov_b32_e32 v1, v157
	v_cvt_pk_fp8_f32 v0, v4, v5 op_sel:[0,0,1]
	v_mul_f32_e32 v4, 0x43800000, v38
	v_cvt_pk_fp8_f32 v1, v2, v4
	v_mul_f32_e32 v5, 0x43800000, v42
	v_mul_f32_e32 v6, 0x43800000, v46
	v_add_co_u32_e32 v4, vcc, s18, v48
	v_cvt_pk_fp8_f32 v1, v5, v6 op_sel:[0,0,1]
	s_nop 0
	v_addc_co_u32_e32 v5, vcc, 0, v49, vcc
	v_mul_f32_e32 v2, 0x43800000, v7
	global_store_dwordx2 v[4:5], v[0:1], off
	v_mul_f32_e32 v1, 0x43800000, v3
	v_mov_b32_e32 v0, v157
	v_cvt_pk_fp8_f32 v0, v1, v2
	v_mul_f32_e32 v3, 0x43800000, v23
	v_mul_f32_e32 v6, 0x43800000, v27
	v_mul_f32_e32 v2, 0x43800000, v35
	v_cvt_pk_fp8_f32 v0, v3, v6 op_sel:[0,0,1]
	v_mul_f32_e32 v3, 0x43800000, v39
	v_mov_b32_e32 v1, v157
	v_cvt_pk_fp8_f32 v1, v2, v3
	v_mul_f32_e32 v6, 0x43800000, v43
	v_mul_f32_e32 v7, 0x43800000, v47
	global_store_dwordx2 v[48:49], v[50:51], off
	v_cvt_pk_fp8_f32 v1, v6, v7 op_sel:[0,0,1]
	v_mov_b64_e32 v[50:51], v[14:15]
	v_mov_b64_e32 v[48:49], v[12:13]
	v_mov_b64_e32 v[52:53], v[8:9]
	global_store_dwordx2 v[4:5], v[0:1], off offset:2048
	s_cbranch_scc1 .LBB0_369
